# v056 + LDS-DMA before fragment reads in K-loop load segments + leading half's alignment barrier inside its epilogue
# speedup vs baseline: 1.0015x; 1.0015x over previous
.LBB0_417:
	s_add_u32 s28, s6, 0xfffc0080
	s_addc_u32 s29, s7, -1
	s_add_i32 s43, 0, 0x10000
	s_cmp_eq_u32 s42, 12
	s_cselect_b32 s31, s5, s29
	s_cselect_b32 s30, s8, s28
	s_cselect_b32 s29, s9, s33
	s_cselect_b32 s28, s21, s23
	s_add_i32 s63, 0, 0x14000
	s_add_i32 m0, s45, 0xc000
	s_nop 0
	global_load_lds_dwordx4 v166, s[6:7]
	s_add_i32 m0, s45, 0xe000
	s_nop 0
	global_load_lds_dwordx4 v164, s[6:7]
	ds_read_b128 v[130:133], v165
	ds_read_b128 v[134:137], v165 offset:1024
	ds_read_b128 v[138:141], v165 offset:2048
	ds_read_b128 v[142:145], v165 offset:3072
	ds_read_b128 v[146:149], v165 offset:16384
	ds_read_b128 v[150:153], v165 offset:17408
	ds_read_b128 v[154:157], v165 offset:18432
	ds_read_b128 v[168:171], v165 offset:19456
	ds_read_b128 v[172:175], v188
	ds_read_b128 v[176:179], v188 offset:1024
	ds_read_b128 v[180:183], v188 offset:2048
	ds_read_b128 v[190:193], v188 offset:3072
	ds_read_b128 v[194:197], v188 offset:4096
	ds_read_b128 v[198:201], v188 offset:5120
	ds_read_b128 v[202:205], v188 offset:6144
	ds_read_b128 v[206:209], v188 offset:7168
	s_waitcnt vmcnt(8) lgkmcnt(0)
	s_barrier
	v_mfma_f32_16x16x32_bf16 v[126:129], v[130:133], v[172:175], v[126:129]
	v_mfma_f32_16x16x32_bf16 v[122:125], v[138:141], v[172:175], v[122:125]
	v_mfma_f32_16x16x32_bf16 v[114:117], v[130:133], v[180:183], v[114:117]
	v_mfma_f32_16x16x32_bf16 v[106:109], v[138:141], v[180:183], v[106:109]
	v_mfma_f32_16x16x32_bf16 v[98:101], v[130:133], v[194:197], v[98:101]
	v_mfma_f32_16x16x32_bf16 v[90:93], v[138:141], v[194:197], v[90:93]
	v_mfma_f32_16x16x32_bf16 v[82:85], v[130:133], v[202:205], v[82:85]
	v_mfma_f32_16x16x32_bf16 v[74:77], v[138:141], v[202:205], v[74:77]
	v_mfma_f32_16x16x32_bf16 v[126:129], v[134:137], v[176:179], v[126:129]
	v_mfma_f32_16x16x32_bf16 v[122:125], v[142:145], v[176:179], v[122:125]
	v_mfma_f32_16x16x32_bf16 v[114:117], v[134:137], v[190:193], v[114:117]
	v_mfma_f32_16x16x32_bf16 v[106:109], v[142:145], v[190:193], v[106:109]
	v_mfma_f32_16x16x32_bf16 v[98:101], v[134:137], v[198:201], v[98:101]
	v_mfma_f32_16x16x32_bf16 v[90:93], v[142:145], v[198:201], v[90:93]
	v_mfma_f32_16x16x32_bf16 v[82:85], v[134:137], v[206:209], v[82:85]
	v_mfma_f32_16x16x32_bf16 v[74:77], v[142:145], v[206:209], v[74:77]
	v_mfma_f32_16x16x32_bf16 v[118:121], v[146:149], v[172:175], v[118:121]
	v_mfma_f32_16x16x32_bf16 v[110:113], v[154:157], v[172:175], v[110:113]
	v_mfma_f32_16x16x32_bf16 v[102:105], v[146:149], v[180:183], v[102:105]
	v_mfma_f32_16x16x32_bf16 v[94:97], v[154:157], v[180:183], v[94:97]
	v_mfma_f32_16x16x32_bf16 v[86:89], v[146:149], v[194:197], v[86:89]
	v_mfma_f32_16x16x32_bf16 v[78:81], v[154:157], v[194:197], v[78:81]
	v_mfma_f32_16x16x32_bf16 v[70:73], v[146:149], v[202:205], v[70:73]
	v_mfma_f32_16x16x32_bf16 v[66:69], v[154:157], v[202:205], v[66:69]
	v_mfma_f32_16x16x32_bf16 v[118:121], v[150:153], v[176:179], v[118:121]
	v_mfma_f32_16x16x32_bf16 v[110:113], v[168:171], v[176:179], v[110:113]
	v_mfma_f32_16x16x32_bf16 v[102:105], v[150:153], v[190:193], v[102:105]
	v_mfma_f32_16x16x32_bf16 v[94:97], v[168:171], v[190:193], v[94:97]
	v_mfma_f32_16x16x32_bf16 v[86:89], v[150:153], v[198:201], v[86:89]
	v_mfma_f32_16x16x32_bf16 v[78:81], v[168:171], v[198:201], v[78:81]
	v_mfma_f32_16x16x32_bf16 v[70:73], v[150:153], v[206:209], v[70:73]
	v_mfma_f32_16x16x32_bf16 v[66:69], v[168:171], v[206:209], v[66:69]
	s_barrier
	s_add_i32 s43, s43, s44
	v_lshl_add_u64 v[216:217], s[28:29], 0, v[0:1]
	s_mov_b32 m0, s43
	s_nop 0
	global_load_lds_dwordx4 v0, s[28:29]
	s_add_i32 m0, s43, 0x2000
	s_add_u32 s58, s28, 0x40000
	v_lshl_add_u64 v[218:219], s[28:29], 0, v[158:159]
	s_addc_u32 s59, s29, 0
	s_add_i32 s43, s63, s44
	global_load_lds_dwordx4 v158, s[28:29]
	s_mov_b32 m0, s43
	v_lshl_add_u64 v[222:223], s[30:31], 0, v[160:161]
	global_load_lds_dwordx4 v0, s[58:59]
	s_add_i32 m0, s43, 0x2000
	s_nop 0
	global_load_lds_dwordx4 v158, s[58:59]
	s_mov_b32 m0, s45
	v_lshl_add_u64 v[220:221], s[30:31], 0, v[162:163]
	global_load_lds_dwordx4 v162, s[30:31]
	s_mov_b32 m0, s46
	s_nop 0
	global_load_lds_dwordx4 v160, s[30:31]
	ds_read_b128 v[172:175], v188 offset:16384
	ds_read_b128 v[176:179], v188 offset:17408
	ds_read_b128 v[180:183], v188 offset:18432
	ds_read_b128 v[190:193], v188 offset:19456
	ds_read_b128 v[194:197], v188 offset:20480
	ds_read_b128 v[198:201], v188 offset:21504
	ds_read_b128 v[202:205], v188 offset:22528
	ds_read_b128 v[206:209], v188 offset:23552
	s_waitcnt vmcnt(8) lgkmcnt(0)
	s_barrier
	v_mfma_f32_16x16x32_bf16 v[62:65], v[130:133], v[172:175], v[62:65]
	v_mfma_f32_16x16x32_bf16 v[58:61], v[138:141], v[172:175], v[58:61]
	v_mfma_f32_16x16x32_bf16 v[50:53], v[130:133], v[180:183], v[50:53]
	v_mfma_f32_16x16x32_bf16 v[42:45], v[138:141], v[180:183], v[42:45]
	v_mfma_f32_16x16x32_bf16 v[34:37], v[130:133], v[194:197], v[34:37]
	v_mfma_f32_16x16x32_bf16 v[26:29], v[138:141], v[194:197], v[26:29]
	v_mfma_f32_16x16x32_bf16 v[18:21], v[130:133], v[202:205], v[18:21]
	v_mfma_f32_16x16x32_bf16 v[10:13], v[138:141], v[202:205], v[10:13]
	v_mfma_f32_16x16x32_bf16 v[62:65], v[134:137], v[176:179], v[62:65]
	v_mfma_f32_16x16x32_bf16 v[58:61], v[142:145], v[176:179], v[58:61]
	v_mfma_f32_16x16x32_bf16 v[50:53], v[134:137], v[190:193], v[50:53]
	v_mfma_f32_16x16x32_bf16 v[42:45], v[142:145], v[190:193], v[42:45]
	v_mfma_f32_16x16x32_bf16 v[34:37], v[134:137], v[198:201], v[34:37]
	v_mfma_f32_16x16x32_bf16 v[26:29], v[142:145], v[198:201], v[26:29]
	v_mfma_f32_16x16x32_bf16 v[18:21], v[134:137], v[206:209], v[18:21]
	v_mfma_f32_16x16x32_bf16 v[10:13], v[142:145], v[206:209], v[10:13]
	v_mfma_f32_16x16x32_bf16 v[54:57], v[146:149], v[172:175], v[54:57]
	v_mfma_f32_16x16x32_bf16 v[46:49], v[154:157], v[172:175], v[46:49]
	v_mfma_f32_16x16x32_bf16 v[38:41], v[146:149], v[180:183], v[38:41]
	v_mfma_f32_16x16x32_bf16 v[30:33], v[154:157], v[180:183], v[30:33]
	v_mfma_f32_16x16x32_bf16 v[22:25], v[146:149], v[194:197], v[22:25]
	v_mfma_f32_16x16x32_bf16 v[14:17], v[154:157], v[194:197], v[14:17]
	v_mfma_f32_16x16x32_bf16 v[6:9], v[146:149], v[202:205], v[6:9]
	v_mfma_f32_16x16x32_bf16 v[2:5], v[154:157], v[202:205], v[2:5]
	v_mfma_f32_16x16x32_bf16 v[54:57], v[150:153], v[176:179], v[54:57]
	v_mfma_f32_16x16x32_bf16 v[46:49], v[168:171], v[176:179], v[46:49]
	v_mfma_f32_16x16x32_bf16 v[38:41], v[150:153], v[190:193], v[38:41]
	v_mfma_f32_16x16x32_bf16 v[30:33], v[168:171], v[190:193], v[30:33]
	v_mfma_f32_16x16x32_bf16 v[22:25], v[150:153], v[198:201], v[22:25]
	v_mfma_f32_16x16x32_bf16 v[14:17], v[168:171], v[198:201], v[14:17]
	v_mfma_f32_16x16x32_bf16 v[6:9], v[150:153], v[206:209], v[6:9]
	v_mfma_f32_16x16x32_bf16 v[2:5], v[168:171], v[206:209], v[2:5]
	s_barrier
	s_add_i32 s43, 0, 0x18000
	s_add_i32 s58, 0, 0x1c000
	s_add_u32 s30, s30, 0x40000
	s_addc_u32 s31, s31, 0
	s_mov_b32 m0, s47
	s_nop 0
	global_load_lds_dwordx4 v162, s[30:31]
	s_mov_b32 m0, s48
	s_nop 0
	global_load_lds_dwordx4 v160, s[30:31]
	ds_read_b128 v[130:133], v165 offset:32768
	ds_read_b128 v[134:137], v165 offset:33792
	ds_read_b128 v[138:141], v165 offset:34816
	ds_read_b128 v[142:145], v165 offset:35840
	ds_read_b128 v[146:149], v165 offset:49152
	ds_read_b128 v[150:153], v165 offset:50176
	ds_read_b128 v[154:157], v165 offset:51200
	ds_read_b128 v[168:171], v165 offset:52224
	ds_read_b128 v[172:175], v188 offset:32768
	ds_read_b128 v[176:179], v188 offset:33792
	ds_read_b128 v[180:183], v188 offset:34816
	ds_read_b128 v[190:193], v188 offset:35840
	ds_read_b128 v[194:197], v188 offset:36864
	ds_read_b128 v[198:201], v188 offset:37888
	ds_read_b128 v[202:205], v188 offset:38912
	ds_read_b128 v[206:209], v188 offset:39936
	s_waitcnt vmcnt(8) lgkmcnt(0)
	s_barrier
	v_mfma_f32_16x16x32_bf16 v[126:129], v[130:133], v[172:175], v[126:129]
	v_mfma_f32_16x16x32_bf16 v[122:125], v[138:141], v[172:175], v[122:125]
	v_mfma_f32_16x16x32_bf16 v[114:117], v[130:133], v[180:183], v[114:117]
	v_mfma_f32_16x16x32_bf16 v[106:109], v[138:141], v[180:183], v[106:109]
	v_mfma_f32_16x16x32_bf16 v[98:101], v[130:133], v[194:197], v[98:101]
	v_mfma_f32_16x16x32_bf16 v[90:93], v[138:141], v[194:197], v[90:93]
	v_mfma_f32_16x16x32_bf16 v[82:85], v[130:133], v[202:205], v[82:85]
	v_mfma_f32_16x16x32_bf16 v[74:77], v[138:141], v[202:205], v[74:77]
	v_mfma_f32_16x16x32_bf16 v[126:129], v[134:137], v[176:179], v[126:129]
	v_mfma_f32_16x16x32_bf16 v[122:125], v[142:145], v[176:179], v[122:125]
	v_mfma_f32_16x16x32_bf16 v[114:117], v[134:137], v[190:193], v[114:117]
	v_mfma_f32_16x16x32_bf16 v[106:109], v[142:145], v[190:193], v[106:109]
	v_mfma_f32_16x16x32_bf16 v[98:101], v[134:137], v[198:201], v[98:101]
	v_mfma_f32_16x16x32_bf16 v[90:93], v[142:145], v[198:201], v[90:93]
	v_mfma_f32_16x16x32_bf16 v[82:85], v[134:137], v[206:209], v[82:85]
	v_mfma_f32_16x16x32_bf16 v[74:77], v[142:145], v[206:209], v[74:77]
	v_mfma_f32_16x16x32_bf16 v[118:121], v[146:149], v[172:175], v[118:121]
	v_mfma_f32_16x16x32_bf16 v[110:113], v[154:157], v[172:175], v[110:113]
	v_mfma_f32_16x16x32_bf16 v[102:105], v[146:149], v[180:183], v[102:105]
	v_mfma_f32_16x16x32_bf16 v[94:97], v[154:157], v[180:183], v[94:97]
	v_mfma_f32_16x16x32_bf16 v[86:89], v[146:149], v[194:197], v[86:89]
	v_mfma_f32_16x16x32_bf16 v[78:81], v[154:157], v[194:197], v[78:81]
	v_mfma_f32_16x16x32_bf16 v[70:73], v[146:149], v[202:205], v[70:73]
	v_mfma_f32_16x16x32_bf16 v[66:69], v[154:157], v[202:205], v[66:69]
	v_mfma_f32_16x16x32_bf16 v[118:121], v[150:153], v[176:179], v[118:121]
	v_mfma_f32_16x16x32_bf16 v[110:113], v[168:171], v[176:179], v[110:113]
	v_mfma_f32_16x16x32_bf16 v[102:105], v[150:153], v[190:193], v[102:105]
	v_mfma_f32_16x16x32_bf16 v[94:97], v[168:171], v[190:193], v[94:97]
	v_mfma_f32_16x16x32_bf16 v[86:89], v[150:153], v[198:201], v[86:89]
	v_mfma_f32_16x16x32_bf16 v[78:81], v[168:171], v[198:201], v[78:81]
	v_mfma_f32_16x16x32_bf16 v[70:73], v[150:153], v[206:209], v[70:73]
	v_mfma_f32_16x16x32_bf16 v[66:69], v[168:171], v[206:209], v[66:69]
	s_barrier
	s_add_i32 s30, s43, s44
	v_lshl_add_u64 v[216:217], v[216:217], 0, s[56:57]
	s_mov_b32 m0, s30
	s_nop 0
	global_load_lds_dwordx4 v[216:217], off
	s_add_i32 m0, s30, 0x2000
	s_add_u32 s28, s28, 0x40080
	v_lshl_add_u64 v[216:217], v[218:219], 0, s[56:57]
	s_addc_u32 s29, s29, 0
	s_add_i32 s30, s58, s44
	global_load_lds_dwordx4 v[216:217], off
	s_mov_b32 m0, s30
	s_nop 0
	global_load_lds_dwordx4 v0, s[28:29]
	s_add_i32 m0, s30, 0x2000
	s_nop 0
	global_load_lds_dwordx4 v158, s[28:29]
	s_mov_b32 m0, s49
	v_lshl_add_u64 v[216:217], v[220:221], 0, s[56:57]
	global_load_lds_dwordx4 v[216:217], off
	s_mov_b32 m0, s52
	v_lshl_add_u64 v[216:217], v[222:223], 0, s[56:57]
	global_load_lds_dwordx4 v[216:217], off
	ds_read_b128 v[172:175], v188 offset:49152
	ds_read_b128 v[176:179], v188 offset:50176
	ds_read_b128 v[180:183], v188 offset:51200
	ds_read_b128 v[190:193], v188 offset:52224
	ds_read_b128 v[194:197], v188 offset:53248
	ds_read_b128 v[198:201], v188 offset:54272
	ds_read_b128 v[202:205], v188 offset:55296
	ds_read_b128 v[206:209], v188 offset:56320
	s_waitcnt vmcnt(8) lgkmcnt(0)
	s_barrier
	v_mfma_f32_16x16x32_bf16 v[62:65], v[130:133], v[172:175], v[62:65]
	v_mfma_f32_16x16x32_bf16 v[58:61], v[138:141], v[172:175], v[58:61]
	v_mfma_f32_16x16x32_bf16 v[50:53], v[130:133], v[180:183], v[50:53]
	v_mfma_f32_16x16x32_bf16 v[42:45], v[138:141], v[180:183], v[42:45]
	v_mfma_f32_16x16x32_bf16 v[34:37], v[130:133], v[194:197], v[34:37]
	v_mfma_f32_16x16x32_bf16 v[26:29], v[138:141], v[194:197], v[26:29]
	v_mfma_f32_16x16x32_bf16 v[18:21], v[130:133], v[202:205], v[18:21]
	v_mfma_f32_16x16x32_bf16 v[10:13], v[138:141], v[202:205], v[10:13]
	v_mfma_f32_16x16x32_bf16 v[62:65], v[134:137], v[176:179], v[62:65]
	v_mfma_f32_16x16x32_bf16 v[58:61], v[142:145], v[176:179], v[58:61]
	v_mfma_f32_16x16x32_bf16 v[50:53], v[134:137], v[190:193], v[50:53]
	v_mfma_f32_16x16x32_bf16 v[42:45], v[142:145], v[190:193], v[42:45]
	v_mfma_f32_16x16x32_bf16 v[34:37], v[134:137], v[198:201], v[34:37]
	v_mfma_f32_16x16x32_bf16 v[26:29], v[142:145], v[198:201], v[26:29]
	v_mfma_f32_16x16x32_bf16 v[18:21], v[134:137], v[206:209], v[18:21]
	v_mfma_f32_16x16x32_bf16 v[10:13], v[142:145], v[206:209], v[10:13]
	v_mfma_f32_16x16x32_bf16 v[54:57], v[146:149], v[172:175], v[54:57]
	v_mfma_f32_16x16x32_bf16 v[46:49], v[154:157], v[172:175], v[46:49]
	v_mfma_f32_16x16x32_bf16 v[38:41], v[146:149], v[180:183], v[38:41]
	v_mfma_f32_16x16x32_bf16 v[30:33], v[154:157], v[180:183], v[30:33]
	v_mfma_f32_16x16x32_bf16 v[22:25], v[146:149], v[194:197], v[22:25]
	v_mfma_f32_16x16x32_bf16 v[14:17], v[154:157], v[194:197], v[14:17]
	v_mfma_f32_16x16x32_bf16 v[6:9], v[146:149], v[202:205], v[6:9]
	v_mfma_f32_16x16x32_bf16 v[2:5], v[154:157], v[202:205], v[2:5]
	v_mfma_f32_16x16x32_bf16 v[54:57], v[150:153], v[176:179], v[54:57]
	v_mfma_f32_16x16x32_bf16 v[46:49], v[168:171], v[176:179], v[46:49]
	v_mfma_f32_16x16x32_bf16 v[38:41], v[150:153], v[190:193], v[38:41]
	v_mfma_f32_16x16x32_bf16 v[30:33], v[168:171], v[190:193], v[30:33]
	v_mfma_f32_16x16x32_bf16 v[22:25], v[150:153], v[198:201], v[22:25]
	v_mfma_f32_16x16x32_bf16 v[14:17], v[168:171], v[198:201], v[14:17]
	v_mfma_f32_16x16x32_bf16 v[6:9], v[150:153], v[206:209], v[6:9]
	v_mfma_f32_16x16x32_bf16 v[2:5], v[168:171], v[206:209], v[2:5]
	s_barrier
	s_add_i32 s42, s42, 2
	s_add_u32 s23, s23, 0x100
	s_addc_u32 s33, s33, 0
	s_add_u32 s6, s6, 0x100
	s_addc_u32 s7, s7, 0
	s_cmp_gt_u32 s42, 13
	s_cbranch_scc0 .LBB0_417



.LBB0_836:
	s_add_u32 s28, s6, 0xfffc0080
	s_addc_u32 s29, s7, -1
	s_add_i32 s41, 0, 0x10000
	s_cmp_eq_u32 s40, 12
	s_cselect_b32 s31, s5, s29
	s_cselect_b32 s30, s8, s28
	s_cselect_b32 s29, s9, s33
	s_cselect_b32 s28, s21, s23
	s_add_i32 s53, 0, 0x14000
	s_add_i32 m0, s43, 0xc000
	s_nop 0
	global_load_lds_dwordx4 v166, s[6:7]
	s_add_i32 m0, s43, 0xe000
	s_nop 0
	global_load_lds_dwordx4 v164, s[6:7]
	ds_read_b128 v[130:133], v165
	ds_read_b128 v[134:137], v165 offset:1024
	ds_read_b128 v[138:141], v165 offset:2048
	ds_read_b128 v[142:145], v165 offset:3072
	ds_read_b128 v[146:149], v165 offset:16384
	ds_read_b128 v[150:153], v165 offset:17408
	ds_read_b128 v[154:157], v165 offset:18432
	ds_read_b128 v[168:171], v165 offset:19456
	ds_read_b128 v[172:175], v188
	ds_read_b128 v[176:179], v188 offset:1024
	ds_read_b128 v[180:183], v188 offset:2048
	ds_read_b128 v[190:193], v188 offset:3072
	ds_read_b128 v[194:197], v188 offset:4096
	ds_read_b128 v[198:201], v188 offset:5120
	ds_read_b128 v[202:205], v188 offset:6144
	ds_read_b128 v[206:209], v188 offset:7168
	s_waitcnt vmcnt(8) lgkmcnt(0)
	s_barrier
	v_mfma_f32_16x16x32_bf16 v[126:129], v[130:133], v[172:175], v[126:129]
	v_mfma_f32_16x16x32_bf16 v[122:125], v[138:141], v[172:175], v[122:125]
	v_mfma_f32_16x16x32_bf16 v[114:117], v[130:133], v[180:183], v[114:117]
	v_mfma_f32_16x16x32_bf16 v[106:109], v[138:141], v[180:183], v[106:109]
	v_mfma_f32_16x16x32_bf16 v[98:101], v[130:133], v[194:197], v[98:101]
	v_mfma_f32_16x16x32_bf16 v[90:93], v[138:141], v[194:197], v[90:93]
	v_mfma_f32_16x16x32_bf16 v[82:85], v[130:133], v[202:205], v[82:85]
	v_mfma_f32_16x16x32_bf16 v[74:77], v[138:141], v[202:205], v[74:77]
	v_mfma_f32_16x16x32_bf16 v[126:129], v[134:137], v[176:179], v[126:129]
	v_mfma_f32_16x16x32_bf16 v[122:125], v[142:145], v[176:179], v[122:125]
	v_mfma_f32_16x16x32_bf16 v[114:117], v[134:137], v[190:193], v[114:117]
	v_mfma_f32_16x16x32_bf16 v[106:109], v[142:145], v[190:193], v[106:109]
	v_mfma_f32_16x16x32_bf16 v[98:101], v[134:137], v[198:201], v[98:101]
	v_mfma_f32_16x16x32_bf16 v[90:93], v[142:145], v[198:201], v[90:93]
	v_mfma_f32_16x16x32_bf16 v[82:85], v[134:137], v[206:209], v[82:85]
	v_mfma_f32_16x16x32_bf16 v[74:77], v[142:145], v[206:209], v[74:77]
	v_mfma_f32_16x16x32_bf16 v[118:121], v[146:149], v[172:175], v[118:121]
	v_mfma_f32_16x16x32_bf16 v[110:113], v[154:157], v[172:175], v[110:113]
	v_mfma_f32_16x16x32_bf16 v[102:105], v[146:149], v[180:183], v[102:105]
	v_mfma_f32_16x16x32_bf16 v[94:97], v[154:157], v[180:183], v[94:97]
	v_mfma_f32_16x16x32_bf16 v[86:89], v[146:149], v[194:197], v[86:89]
	v_mfma_f32_16x16x32_bf16 v[78:81], v[154:157], v[194:197], v[78:81]
	v_mfma_f32_16x16x32_bf16 v[70:73], v[146:149], v[202:205], v[70:73]
	v_mfma_f32_16x16x32_bf16 v[66:69], v[154:157], v[202:205], v[66:69]
	v_mfma_f32_16x16x32_bf16 v[118:121], v[150:153], v[176:179], v[118:121]
	v_mfma_f32_16x16x32_bf16 v[110:113], v[168:171], v[176:179], v[110:113]
	v_mfma_f32_16x16x32_bf16 v[102:105], v[150:153], v[190:193], v[102:105]
	v_mfma_f32_16x16x32_bf16 v[94:97], v[168:171], v[190:193], v[94:97]
	v_mfma_f32_16x16x32_bf16 v[86:89], v[150:153], v[198:201], v[86:89]
	v_mfma_f32_16x16x32_bf16 v[78:81], v[168:171], v[198:201], v[78:81]
	v_mfma_f32_16x16x32_bf16 v[70:73], v[150:153], v[206:209], v[70:73]
	v_mfma_f32_16x16x32_bf16 v[66:69], v[168:171], v[206:209], v[66:69]
	s_barrier
	s_add_i32 s41, s41, s42
	v_lshl_add_u64 v[216:217], s[28:29], 0, v[0:1]
	s_mov_b32 m0, s41
	s_nop 0
	global_load_lds_dwordx4 v0, s[28:29]
	s_add_i32 m0, s41, 0x2000
	s_add_u32 s58, s28, 0x40000
	v_lshl_add_u64 v[218:219], s[28:29], 0, v[158:159]
	s_addc_u32 s59, s29, 0
	s_add_i32 s41, s53, s42
	global_load_lds_dwordx4 v158, s[28:29]
	s_mov_b32 m0, s41
	v_lshl_add_u64 v[222:223], s[30:31], 0, v[160:161]
	global_load_lds_dwordx4 v0, s[58:59]
	s_add_i32 m0, s41, 0x2000
	s_nop 0
	global_load_lds_dwordx4 v158, s[58:59]
	s_mov_b32 m0, s43
	v_lshl_add_u64 v[220:221], s[30:31], 0, v[162:163]
	global_load_lds_dwordx4 v162, s[30:31]
	s_mov_b32 m0, s44
	s_nop 0
	global_load_lds_dwordx4 v160, s[30:31]
	ds_read_b128 v[172:175], v188 offset:16384
	ds_read_b128 v[176:179], v188 offset:17408
	ds_read_b128 v[180:183], v188 offset:18432
	ds_read_b128 v[190:193], v188 offset:19456
	ds_read_b128 v[194:197], v188 offset:20480
	ds_read_b128 v[198:201], v188 offset:21504
	ds_read_b128 v[202:205], v188 offset:22528
	ds_read_b128 v[206:209], v188 offset:23552
	s_waitcnt vmcnt(8) lgkmcnt(0)
	s_barrier
	v_mfma_f32_16x16x32_bf16 v[62:65], v[130:133], v[172:175], v[62:65]
	v_mfma_f32_16x16x32_bf16 v[58:61], v[138:141], v[172:175], v[58:61]
	v_mfma_f32_16x16x32_bf16 v[50:53], v[130:133], v[180:183], v[50:53]
	v_mfma_f32_16x16x32_bf16 v[42:45], v[138:141], v[180:183], v[42:45]
	v_mfma_f32_16x16x32_bf16 v[34:37], v[130:133], v[194:197], v[34:37]
	v_mfma_f32_16x16x32_bf16 v[26:29], v[138:141], v[194:197], v[26:29]
	v_mfma_f32_16x16x32_bf16 v[18:21], v[130:133], v[202:205], v[18:21]
	v_mfma_f32_16x16x32_bf16 v[10:13], v[138:141], v[202:205], v[10:13]
	v_mfma_f32_16x16x32_bf16 v[62:65], v[134:137], v[176:179], v[62:65]
	v_mfma_f32_16x16x32_bf16 v[58:61], v[142:145], v[176:179], v[58:61]
	v_mfma_f32_16x16x32_bf16 v[50:53], v[134:137], v[190:193], v[50:53]
	v_mfma_f32_16x16x32_bf16 v[42:45], v[142:145], v[190:193], v[42:45]
	v_mfma_f32_16x16x32_bf16 v[34:37], v[134:137], v[198:201], v[34:37]
	v_mfma_f32_16x16x32_bf16 v[26:29], v[142:145], v[198:201], v[26:29]
	v_mfma_f32_16x16x32_bf16 v[18:21], v[134:137], v[206:209], v[18:21]
	v_mfma_f32_16x16x32_bf16 v[10:13], v[142:145], v[206:209], v[10:13]
	v_mfma_f32_16x16x32_bf16 v[54:57], v[146:149], v[172:175], v[54:57]
	v_mfma_f32_16x16x32_bf16 v[46:49], v[154:157], v[172:175], v[46:49]
	v_mfma_f32_16x16x32_bf16 v[38:41], v[146:149], v[180:183], v[38:41]
	v_mfma_f32_16x16x32_bf16 v[30:33], v[154:157], v[180:183], v[30:33]
	v_mfma_f32_16x16x32_bf16 v[22:25], v[146:149], v[194:197], v[22:25]
	v_mfma_f32_16x16x32_bf16 v[14:17], v[154:157], v[194:197], v[14:17]
	v_mfma_f32_16x16x32_bf16 v[6:9], v[146:149], v[202:205], v[6:9]
	v_mfma_f32_16x16x32_bf16 v[2:5], v[154:157], v[202:205], v[2:5]
	v_mfma_f32_16x16x32_bf16 v[54:57], v[150:153], v[176:179], v[54:57]
	v_mfma_f32_16x16x32_bf16 v[46:49], v[168:171], v[176:179], v[46:49]
	v_mfma_f32_16x16x32_bf16 v[38:41], v[150:153], v[190:193], v[38:41]
	v_mfma_f32_16x16x32_bf16 v[30:33], v[168:171], v[190:193], v[30:33]
	v_mfma_f32_16x16x32_bf16 v[22:25], v[150:153], v[198:201], v[22:25]
	v_mfma_f32_16x16x32_bf16 v[14:17], v[168:171], v[198:201], v[14:17]
	v_mfma_f32_16x16x32_bf16 v[6:9], v[150:153], v[206:209], v[6:9]
	v_mfma_f32_16x16x32_bf16 v[2:5], v[168:171], v[206:209], v[2:5]
	s_barrier
	s_add_i32 s41, 0, 0x18000
	s_add_i32 s53, 0, 0x1c000
	s_add_u32 s30, s30, 0x40000
	s_addc_u32 s31, s31, 0
	s_mov_b32 m0, s45
	s_nop 0
	global_load_lds_dwordx4 v162, s[30:31]
	s_mov_b32 m0, s46
	s_nop 0
	global_load_lds_dwordx4 v160, s[30:31]
	ds_read_b128 v[130:133], v165 offset:32768
	ds_read_b128 v[134:137], v165 offset:33792
	ds_read_b128 v[138:141], v165 offset:34816
	ds_read_b128 v[142:145], v165 offset:35840
	ds_read_b128 v[146:149], v165 offset:49152
	ds_read_b128 v[150:153], v165 offset:50176
	ds_read_b128 v[154:157], v165 offset:51200
	ds_read_b128 v[168:171], v165 offset:52224
	ds_read_b128 v[172:175], v188 offset:32768
	ds_read_b128 v[176:179], v188 offset:33792
	ds_read_b128 v[180:183], v188 offset:34816
	ds_read_b128 v[190:193], v188 offset:35840
	ds_read_b128 v[194:197], v188 offset:36864
	ds_read_b128 v[198:201], v188 offset:37888
	ds_read_b128 v[202:205], v188 offset:38912
	ds_read_b128 v[206:209], v188 offset:39936
	s_waitcnt vmcnt(8) lgkmcnt(0)
	s_barrier
	v_mfma_f32_16x16x32_bf16 v[126:129], v[130:133], v[172:175], v[126:129]
	v_mfma_f32_16x16x32_bf16 v[122:125], v[138:141], v[172:175], v[122:125]
	v_mfma_f32_16x16x32_bf16 v[114:117], v[130:133], v[180:183], v[114:117]
	v_mfma_f32_16x16x32_bf16 v[106:109], v[138:141], v[180:183], v[106:109]
	v_mfma_f32_16x16x32_bf16 v[98:101], v[130:133], v[194:197], v[98:101]
	v_mfma_f32_16x16x32_bf16 v[90:93], v[138:141], v[194:197], v[90:93]
	v_mfma_f32_16x16x32_bf16 v[82:85], v[130:133], v[202:205], v[82:85]
	v_mfma_f32_16x16x32_bf16 v[74:77], v[138:141], v[202:205], v[74:77]
	v_mfma_f32_16x16x32_bf16 v[126:129], v[134:137], v[176:179], v[126:129]
	v_mfma_f32_16x16x32_bf16 v[122:125], v[142:145], v[176:179], v[122:125]
	v_mfma_f32_16x16x32_bf16 v[114:117], v[134:137], v[190:193], v[114:117]
	v_mfma_f32_16x16x32_bf16 v[106:109], v[142:145], v[190:193], v[106:109]
	v_mfma_f32_16x16x32_bf16 v[98:101], v[134:137], v[198:201], v[98:101]
	v_mfma_f32_16x16x32_bf16 v[90:93], v[142:145], v[198:201], v[90:93]
	v_mfma_f32_16x16x32_bf16 v[82:85], v[134:137], v[206:209], v[82:85]
	v_mfma_f32_16x16x32_bf16 v[74:77], v[142:145], v[206:209], v[74:77]
	v_mfma_f32_16x16x32_bf16 v[118:121], v[146:149], v[172:175], v[118:121]
	v_mfma_f32_16x16x32_bf16 v[110:113], v[154:157], v[172:175], v[110:113]
	v_mfma_f32_16x16x32_bf16 v[102:105], v[146:149], v[180:183], v[102:105]
	v_mfma_f32_16x16x32_bf16 v[94:97], v[154:157], v[180:183], v[94:97]
	v_mfma_f32_16x16x32_bf16 v[86:89], v[146:149], v[194:197], v[86:89]
	v_mfma_f32_16x16x32_bf16 v[78:81], v[154:157], v[194:197], v[78:81]
	v_mfma_f32_16x16x32_bf16 v[70:73], v[146:149], v[202:205], v[70:73]
	v_mfma_f32_16x16x32_bf16 v[66:69], v[154:157], v[202:205], v[66:69]
	v_mfma_f32_16x16x32_bf16 v[118:121], v[150:153], v[176:179], v[118:121]
	v_mfma_f32_16x16x32_bf16 v[110:113], v[168:171], v[176:179], v[110:113]
	v_mfma_f32_16x16x32_bf16 v[102:105], v[150:153], v[190:193], v[102:105]
	v_mfma_f32_16x16x32_bf16 v[94:97], v[168:171], v[190:193], v[94:97]
	v_mfma_f32_16x16x32_bf16 v[86:89], v[150:153], v[198:201], v[86:89]
	v_mfma_f32_16x16x32_bf16 v[78:81], v[168:171], v[198:201], v[78:81]
	v_mfma_f32_16x16x32_bf16 v[70:73], v[150:153], v[206:209], v[70:73]
	v_mfma_f32_16x16x32_bf16 v[66:69], v[168:171], v[206:209], v[66:69]
	s_barrier
	s_add_i32 s30, s41, s42
	v_lshl_add_u64 v[216:217], v[216:217], 0, s[56:57]
	s_mov_b32 m0, s30
	s_nop 0
	global_load_lds_dwordx4 v[216:217], off
	s_add_i32 m0, s30, 0x2000
	s_add_u32 s28, s28, 0x40080
	v_lshl_add_u64 v[216:217], v[218:219], 0, s[56:57]
	s_addc_u32 s29, s29, 0
	s_add_i32 s30, s53, s42
	global_load_lds_dwordx4 v[216:217], off
	s_mov_b32 m0, s30
	s_nop 0
	global_load_lds_dwordx4 v0, s[28:29]
	s_add_i32 m0, s30, 0x2000
	s_nop 0
	global_load_lds_dwordx4 v158, s[28:29]
	s_mov_b32 m0, s47
	v_lshl_add_u64 v[216:217], v[220:221], 0, s[56:57]
	global_load_lds_dwordx4 v[216:217], off
	s_mov_b32 m0, s48
	v_lshl_add_u64 v[216:217], v[222:223], 0, s[56:57]
	global_load_lds_dwordx4 v[216:217], off
	ds_read_b128 v[172:175], v188 offset:49152
	ds_read_b128 v[176:179], v188 offset:50176
	ds_read_b128 v[180:183], v188 offset:51200
	ds_read_b128 v[190:193], v188 offset:52224
	ds_read_b128 v[194:197], v188 offset:53248
	ds_read_b128 v[198:201], v188 offset:54272
	ds_read_b128 v[202:205], v188 offset:55296
	ds_read_b128 v[206:209], v188 offset:56320
	s_waitcnt vmcnt(8) lgkmcnt(0)
	s_barrier
	v_mfma_f32_16x16x32_bf16 v[62:65], v[130:133], v[172:175], v[62:65]
	v_mfma_f32_16x16x32_bf16 v[58:61], v[138:141], v[172:175], v[58:61]
	v_mfma_f32_16x16x32_bf16 v[50:53], v[130:133], v[180:183], v[50:53]
	v_mfma_f32_16x16x32_bf16 v[42:45], v[138:141], v[180:183], v[42:45]
	v_mfma_f32_16x16x32_bf16 v[34:37], v[130:133], v[194:197], v[34:37]
	v_mfma_f32_16x16x32_bf16 v[26:29], v[138:141], v[194:197], v[26:29]
	v_mfma_f32_16x16x32_bf16 v[18:21], v[130:133], v[202:205], v[18:21]
	v_mfma_f32_16x16x32_bf16 v[10:13], v[138:141], v[202:205], v[10:13]
	v_mfma_f32_16x16x32_bf16 v[62:65], v[134:137], v[176:179], v[62:65]
	v_mfma_f32_16x16x32_bf16 v[58:61], v[142:145], v[176:179], v[58:61]
	v_mfma_f32_16x16x32_bf16 v[50:53], v[134:137], v[190:193], v[50:53]
	v_mfma_f32_16x16x32_bf16 v[42:45], v[142:145], v[190:193], v[42:45]
	v_mfma_f32_16x16x32_bf16 v[34:37], v[134:137], v[198:201], v[34:37]
	v_mfma_f32_16x16x32_bf16 v[26:29], v[142:145], v[198:201], v[26:29]
	v_mfma_f32_16x16x32_bf16 v[18:21], v[134:137], v[206:209], v[18:21]
	v_mfma_f32_16x16x32_bf16 v[10:13], v[142:145], v[206:209], v[10:13]
	v_mfma_f32_16x16x32_bf16 v[54:57], v[146:149], v[172:175], v[54:57]
	v_mfma_f32_16x16x32_bf16 v[46:49], v[154:157], v[172:175], v[46:49]
	v_mfma_f32_16x16x32_bf16 v[38:41], v[146:149], v[180:183], v[38:41]
	v_mfma_f32_16x16x32_bf16 v[30:33], v[154:157], v[180:183], v[30:33]
	v_mfma_f32_16x16x32_bf16 v[22:25], v[146:149], v[194:197], v[22:25]
	v_mfma_f32_16x16x32_bf16 v[14:17], v[154:157], v[194:197], v[14:17]
	v_mfma_f32_16x16x32_bf16 v[6:9], v[146:149], v[202:205], v[6:9]
	v_mfma_f32_16x16x32_bf16 v[2:5], v[154:157], v[202:205], v[2:5]
	v_mfma_f32_16x16x32_bf16 v[54:57], v[150:153], v[176:179], v[54:57]
	v_mfma_f32_16x16x32_bf16 v[46:49], v[168:171], v[176:179], v[46:49]
	v_mfma_f32_16x16x32_bf16 v[38:41], v[150:153], v[190:193], v[38:41]
	v_mfma_f32_16x16x32_bf16 v[30:33], v[168:171], v[190:193], v[30:33]
	v_mfma_f32_16x16x32_bf16 v[22:25], v[150:153], v[198:201], v[22:25]
	v_mfma_f32_16x16x32_bf16 v[14:17], v[168:171], v[198:201], v[14:17]
	v_mfma_f32_16x16x32_bf16 v[6:9], v[150:153], v[206:209], v[6:9]
	v_mfma_f32_16x16x32_bf16 v[2:5], v[168:171], v[206:209], v[2:5]
	s_barrier
	s_add_i32 s40, s40, 2
	s_add_u32 s23, s23, 0x100
	s_addc_u32 s33, s33, 0
	s_add_u32 s6, s6, 0x100
	s_addc_u32 s7, s7, 0
	s_cmp_gt_u32 s40, 13
	s_cbranch_scc0 .LBB0_836



.LBB0_2626:
	s_add_u32 s26, s6, 0xfffc0080
	s_addc_u32 s27, s7, -1
	s_add_i32 s50, 0, 0x10000
	s_cmp_eq_u32 s49, 12
	s_cselect_b32 s29, s21, s27
	s_cselect_b32 s28, s33, s26
	s_cselect_b32 s27, s19, s48
	s_cselect_b32 s26, s40, s41
	s_add_i32 s58, 0, 0x14000
	s_add_i32 m0, s36, 0xc000
	s_nop 0
	global_load_lds_dwordx4 v168, s[6:7]
	s_add_i32 m0, s36, 0xe000
	s_nop 0
	global_load_lds_dwordx4 v166, s[6:7]
	ds_read_b128 v[130:133], v167
	ds_read_b128 v[134:137], v167 offset:1024
	ds_read_b128 v[138:141], v167 offset:2048
	ds_read_b128 v[142:145], v167 offset:3072
	ds_read_b128 v[146:149], v167 offset:16384
	ds_read_b128 v[150:153], v167 offset:17408
	ds_read_b128 v[154:157], v167 offset:18432
	ds_read_b128 v[170:173], v167 offset:19456
	ds_read_b128 v[174:177], v183
	ds_read_b128 v[184:187], v183 offset:1024
	ds_read_b128 v[188:191], v183 offset:2048
	ds_read_b128 v[192:195], v183 offset:3072
	ds_read_b128 v[196:199], v183 offset:4096
	ds_read_b128 v[200:203], v183 offset:5120
	ds_read_b128 v[204:207], v183 offset:6144
	ds_read_b128 v[216:219], v183 offset:7168
	s_waitcnt vmcnt(8) lgkmcnt(0)
	s_barrier
	v_mfma_f32_16x16x32_bf16 v[126:129], v[130:133], v[174:177], v[126:129]
	v_mfma_f32_16x16x32_bf16 v[122:125], v[138:141], v[174:177], v[122:125]
	v_mfma_f32_16x16x32_bf16 v[110:113], v[130:133], v[188:191], v[110:113]
	v_mfma_f32_16x16x32_bf16 v[106:109], v[138:141], v[188:191], v[106:109]
	v_mfma_f32_16x16x32_bf16 v[94:97], v[130:133], v[196:199], v[94:97]
	v_mfma_f32_16x16x32_bf16 v[90:93], v[138:141], v[196:199], v[90:93]
	v_mfma_f32_16x16x32_bf16 v[78:81], v[130:133], v[204:207], v[78:81]
	v_mfma_f32_16x16x32_bf16 v[74:77], v[138:141], v[204:207], v[74:77]
	v_mfma_f32_16x16x32_bf16 v[126:129], v[134:137], v[184:187], v[126:129]
	v_mfma_f32_16x16x32_bf16 v[122:125], v[142:145], v[184:187], v[122:125]
	v_mfma_f32_16x16x32_bf16 v[110:113], v[134:137], v[192:195], v[110:113]
	v_mfma_f32_16x16x32_bf16 v[106:109], v[142:145], v[192:195], v[106:109]
	v_mfma_f32_16x16x32_bf16 v[94:97], v[134:137], v[200:203], v[94:97]
	v_mfma_f32_16x16x32_bf16 v[90:93], v[142:145], v[200:203], v[90:93]
	v_mfma_f32_16x16x32_bf16 v[78:81], v[134:137], v[216:219], v[78:81]
	v_mfma_f32_16x16x32_bf16 v[74:77], v[142:145], v[216:219], v[74:77]
	v_mfma_f32_16x16x32_bf16 v[118:121], v[146:149], v[174:177], v[118:121]
	v_mfma_f32_16x16x32_bf16 v[114:117], v[154:157], v[174:177], v[114:117]
	v_mfma_f32_16x16x32_bf16 v[102:105], v[146:149], v[188:191], v[102:105]
	v_mfma_f32_16x16x32_bf16 v[98:101], v[154:157], v[188:191], v[98:101]
	v_mfma_f32_16x16x32_bf16 v[86:89], v[146:149], v[196:199], v[86:89]
	v_mfma_f32_16x16x32_bf16 v[82:85], v[154:157], v[196:199], v[82:85]
	v_mfma_f32_16x16x32_bf16 v[70:73], v[146:149], v[204:207], v[70:73]
	v_mfma_f32_16x16x32_bf16 v[66:69], v[154:157], v[204:207], v[66:69]
	v_mfma_f32_16x16x32_bf16 v[118:121], v[150:153], v[184:187], v[118:121]
	v_mfma_f32_16x16x32_bf16 v[114:117], v[170:173], v[184:187], v[114:117]
	v_mfma_f32_16x16x32_bf16 v[102:105], v[150:153], v[192:195], v[102:105]
	v_mfma_f32_16x16x32_bf16 v[98:101], v[170:173], v[192:195], v[98:101]
	v_mfma_f32_16x16x32_bf16 v[86:89], v[150:153], v[200:203], v[86:89]
	v_mfma_f32_16x16x32_bf16 v[82:85], v[170:173], v[200:203], v[82:85]
	v_mfma_f32_16x16x32_bf16 v[70:73], v[150:153], v[216:219], v[70:73]
	v_mfma_f32_16x16x32_bf16 v[66:69], v[170:173], v[216:219], v[66:69]
	s_barrier
	s_add_i32 s50, s50, s35
	v_lshl_add_u64 v[178:179], s[26:27], 0, v[162:163]
	s_mov_b32 m0, s50
	s_nop 0
	global_load_lds_dwordx4 v162, s[26:27]
	s_add_i32 m0, s50, 0x2000
	s_add_u32 s52, s26, 0x40000
	v_lshl_add_u64 v[208:209], s[26:27], 0, v[158:159]
	s_addc_u32 s53, s27, 0
	s_add_i32 s50, s58, s35
	global_load_lds_dwordx4 v158, s[26:27]
	s_mov_b32 m0, s50
	v_lshl_add_u64 v[222:223], s[28:29], 0, v[160:161]
	global_load_lds_dwordx4 v162, s[52:53]
	s_add_i32 m0, s50, 0x2000
	s_nop 0
	global_load_lds_dwordx4 v158, s[52:53]
	s_mov_b32 m0, s36
	v_lshl_add_u64 v[220:221], s[28:29], 0, v[164:165]
	global_load_lds_dwordx4 v164, s[28:29]
	s_mov_b32 m0, s37
	s_nop 0
	global_load_lds_dwordx4 v160, s[28:29]
	ds_read_b128 v[174:177], v183 offset:16384
	ds_read_b128 v[184:187], v183 offset:17408
	ds_read_b128 v[188:191], v183 offset:18432
	ds_read_b128 v[192:195], v183 offset:19456
	ds_read_b128 v[196:199], v183 offset:20480
	ds_read_b128 v[200:203], v183 offset:21504
	ds_read_b128 v[204:207], v183 offset:22528
	ds_read_b128 v[216:219], v183 offset:23552
	s_waitcnt vmcnt(8) lgkmcnt(0)
	s_barrier
	v_mfma_f32_16x16x32_bf16 v[62:65], v[130:133], v[174:177], v[62:65]
	v_mfma_f32_16x16x32_bf16 v[58:61], v[138:141], v[174:177], v[58:61]
	v_mfma_f32_16x16x32_bf16 v[46:49], v[130:133], v[188:191], v[46:49]
	v_mfma_f32_16x16x32_bf16 v[42:45], v[138:141], v[188:191], v[42:45]
	v_mfma_f32_16x16x32_bf16 v[30:33], v[130:133], v[196:199], v[30:33]
	v_mfma_f32_16x16x32_bf16 v[26:29], v[138:141], v[196:199], v[26:29]
	v_mfma_f32_16x16x32_bf16 v[14:17], v[130:133], v[204:207], v[14:17]
	v_mfma_f32_16x16x32_bf16 v[10:13], v[138:141], v[204:207], v[10:13]
	v_mfma_f32_16x16x32_bf16 v[62:65], v[134:137], v[184:187], v[62:65]
	v_mfma_f32_16x16x32_bf16 v[58:61], v[142:145], v[184:187], v[58:61]
	v_mfma_f32_16x16x32_bf16 v[46:49], v[134:137], v[192:195], v[46:49]
	v_mfma_f32_16x16x32_bf16 v[42:45], v[142:145], v[192:195], v[42:45]
	v_mfma_f32_16x16x32_bf16 v[30:33], v[134:137], v[200:203], v[30:33]
	v_mfma_f32_16x16x32_bf16 v[26:29], v[142:145], v[200:203], v[26:29]
	v_mfma_f32_16x16x32_bf16 v[14:17], v[134:137], v[216:219], v[14:17]
	v_mfma_f32_16x16x32_bf16 v[10:13], v[142:145], v[216:219], v[10:13]
	v_mfma_f32_16x16x32_bf16 v[54:57], v[146:149], v[174:177], v[54:57]
	v_mfma_f32_16x16x32_bf16 v[50:53], v[154:157], v[174:177], v[50:53]
	v_mfma_f32_16x16x32_bf16 v[38:41], v[146:149], v[188:191], v[38:41]
	v_mfma_f32_16x16x32_bf16 v[34:37], v[154:157], v[188:191], v[34:37]
	v_mfma_f32_16x16x32_bf16 v[22:25], v[146:149], v[196:199], v[22:25]
	v_mfma_f32_16x16x32_bf16 v[18:21], v[154:157], v[196:199], v[18:21]
	v_mfma_f32_16x16x32_bf16 v[6:9], v[146:149], v[204:207], v[6:9]
	v_mfma_f32_16x16x32_bf16 v[2:5], v[154:157], v[204:207], v[2:5]
	v_mfma_f32_16x16x32_bf16 v[54:57], v[150:153], v[184:187], v[54:57]
	v_mfma_f32_16x16x32_bf16 v[50:53], v[170:173], v[184:187], v[50:53]
	v_mfma_f32_16x16x32_bf16 v[38:41], v[150:153], v[192:195], v[38:41]
	v_mfma_f32_16x16x32_bf16 v[34:37], v[170:173], v[192:195], v[34:37]
	v_mfma_f32_16x16x32_bf16 v[22:25], v[150:153], v[200:203], v[22:25]
	v_mfma_f32_16x16x32_bf16 v[18:21], v[170:173], v[200:203], v[18:21]
	v_mfma_f32_16x16x32_bf16 v[6:9], v[150:153], v[216:219], v[6:9]
	v_mfma_f32_16x16x32_bf16 v[2:5], v[170:173], v[216:219], v[2:5]
	s_barrier
	s_add_i32 s50, 0, 0x18000
	s_add_i32 s52, 0, 0x1c000
	s_add_u32 s28, s28, 0x40000
	s_addc_u32 s29, s29, 0
	s_mov_b32 m0, s42
	s_nop 0
	global_load_lds_dwordx4 v164, s[28:29]
	s_mov_b32 m0, s43
	s_nop 0
	global_load_lds_dwordx4 v160, s[28:29]
	ds_read_b128 v[130:133], v167 offset:32768
	ds_read_b128 v[134:137], v167 offset:33792
	ds_read_b128 v[138:141], v167 offset:34816
	ds_read_b128 v[142:145], v167 offset:35840
	ds_read_b128 v[146:149], v167 offset:49152
	ds_read_b128 v[150:153], v167 offset:50176
	ds_read_b128 v[154:157], v167 offset:51200
	ds_read_b128 v[170:173], v167 offset:52224
	ds_read_b128 v[174:177], v183 offset:32768
	ds_read_b128 v[184:187], v183 offset:33792
	ds_read_b128 v[188:191], v183 offset:34816
	ds_read_b128 v[192:195], v183 offset:35840
	ds_read_b128 v[196:199], v183 offset:36864
	ds_read_b128 v[200:203], v183 offset:37888
	ds_read_b128 v[204:207], v183 offset:38912
	ds_read_b128 v[216:219], v183 offset:39936
	s_waitcnt vmcnt(8) lgkmcnt(0)
	s_barrier
	v_mfma_f32_16x16x32_bf16 v[126:129], v[130:133], v[174:177], v[126:129]
	v_mfma_f32_16x16x32_bf16 v[122:125], v[138:141], v[174:177], v[122:125]
	v_mfma_f32_16x16x32_bf16 v[110:113], v[130:133], v[188:191], v[110:113]
	v_mfma_f32_16x16x32_bf16 v[106:109], v[138:141], v[188:191], v[106:109]
	v_mfma_f32_16x16x32_bf16 v[94:97], v[130:133], v[196:199], v[94:97]
	v_mfma_f32_16x16x32_bf16 v[90:93], v[138:141], v[196:199], v[90:93]
	v_mfma_f32_16x16x32_bf16 v[78:81], v[130:133], v[204:207], v[78:81]
	v_mfma_f32_16x16x32_bf16 v[74:77], v[138:141], v[204:207], v[74:77]
	v_mfma_f32_16x16x32_bf16 v[126:129], v[134:137], v[184:187], v[126:129]
	v_mfma_f32_16x16x32_bf16 v[122:125], v[142:145], v[184:187], v[122:125]
	v_mfma_f32_16x16x32_bf16 v[110:113], v[134:137], v[192:195], v[110:113]
	v_mfma_f32_16x16x32_bf16 v[106:109], v[142:145], v[192:195], v[106:109]
	v_mfma_f32_16x16x32_bf16 v[94:97], v[134:137], v[200:203], v[94:97]
	v_mfma_f32_16x16x32_bf16 v[90:93], v[142:145], v[200:203], v[90:93]
	v_mfma_f32_16x16x32_bf16 v[78:81], v[134:137], v[216:219], v[78:81]
	v_mfma_f32_16x16x32_bf16 v[74:77], v[142:145], v[216:219], v[74:77]
	v_mfma_f32_16x16x32_bf16 v[118:121], v[146:149], v[174:177], v[118:121]
	v_mfma_f32_16x16x32_bf16 v[114:117], v[154:157], v[174:177], v[114:117]
	v_mfma_f32_16x16x32_bf16 v[102:105], v[146:149], v[188:191], v[102:105]
	v_mfma_f32_16x16x32_bf16 v[98:101], v[154:157], v[188:191], v[98:101]
	v_mfma_f32_16x16x32_bf16 v[86:89], v[146:149], v[196:199], v[86:89]
	v_mfma_f32_16x16x32_bf16 v[82:85], v[154:157], v[196:199], v[82:85]
	v_mfma_f32_16x16x32_bf16 v[70:73], v[146:149], v[204:207], v[70:73]
	v_mfma_f32_16x16x32_bf16 v[66:69], v[154:157], v[204:207], v[66:69]
	v_mfma_f32_16x16x32_bf16 v[118:121], v[150:153], v[184:187], v[118:121]
	v_mfma_f32_16x16x32_bf16 v[114:117], v[170:173], v[184:187], v[114:117]
	v_mfma_f32_16x16x32_bf16 v[102:105], v[150:153], v[192:195], v[102:105]
	v_mfma_f32_16x16x32_bf16 v[98:101], v[170:173], v[192:195], v[98:101]
	v_mfma_f32_16x16x32_bf16 v[86:89], v[150:153], v[200:203], v[86:89]
	v_mfma_f32_16x16x32_bf16 v[82:85], v[170:173], v[200:203], v[82:85]
	v_mfma_f32_16x16x32_bf16 v[70:73], v[150:153], v[216:219], v[70:73]
	v_mfma_f32_16x16x32_bf16 v[66:69], v[170:173], v[216:219], v[66:69]
	s_barrier
	s_add_i32 s28, s50, s35
	v_lshl_add_u64 v[178:179], v[178:179], 0, s[56:57]
	s_mov_b32 m0, s28
	s_nop 0
	global_load_lds_dwordx4 v[178:179], off
	s_add_i32 m0, s28, 0x2000
	s_add_u32 s26, s26, 0x40080
	v_lshl_add_u64 v[178:179], v[208:209], 0, s[56:57]
	s_addc_u32 s27, s27, 0
	s_add_i32 s28, s52, s35
	global_load_lds_dwordx4 v[178:179], off
	s_mov_b32 m0, s28
	s_nop 0
	global_load_lds_dwordx4 v162, s[26:27]
	s_add_i32 m0, s28, 0x2000
	s_nop 0
	global_load_lds_dwordx4 v158, s[26:27]
	s_mov_b32 m0, s44
	v_lshl_add_u64 v[178:179], v[220:221], 0, s[56:57]
	global_load_lds_dwordx4 v[178:179], off
	s_mov_b32 m0, s45
	v_lshl_add_u64 v[178:179], v[222:223], 0, s[56:57]
	global_load_lds_dwordx4 v[178:179], off
	ds_read_b128 v[174:177], v183 offset:49152
	ds_read_b128 v[184:187], v183 offset:50176
	ds_read_b128 v[188:191], v183 offset:51200
	ds_read_b128 v[192:195], v183 offset:52224
	ds_read_b128 v[196:199], v183 offset:53248
	ds_read_b128 v[200:203], v183 offset:54272
	ds_read_b128 v[204:207], v183 offset:55296
	ds_read_b128 v[216:219], v183 offset:56320
	s_waitcnt vmcnt(8) lgkmcnt(0)
	s_barrier
	v_mfma_f32_16x16x32_bf16 v[62:65], v[130:133], v[174:177], v[62:65]
	v_mfma_f32_16x16x32_bf16 v[58:61], v[138:141], v[174:177], v[58:61]
	v_mfma_f32_16x16x32_bf16 v[46:49], v[130:133], v[188:191], v[46:49]
	v_mfma_f32_16x16x32_bf16 v[42:45], v[138:141], v[188:191], v[42:45]
	v_mfma_f32_16x16x32_bf16 v[30:33], v[130:133], v[196:199], v[30:33]
	v_mfma_f32_16x16x32_bf16 v[26:29], v[138:141], v[196:199], v[26:29]
	v_mfma_f32_16x16x32_bf16 v[14:17], v[130:133], v[204:207], v[14:17]
	v_mfma_f32_16x16x32_bf16 v[10:13], v[138:141], v[204:207], v[10:13]
	v_mfma_f32_16x16x32_bf16 v[62:65], v[134:137], v[184:187], v[62:65]
	v_mfma_f32_16x16x32_bf16 v[58:61], v[142:145], v[184:187], v[58:61]
	v_mfma_f32_16x16x32_bf16 v[46:49], v[134:137], v[192:195], v[46:49]
	v_mfma_f32_16x16x32_bf16 v[42:45], v[142:145], v[192:195], v[42:45]
	v_mfma_f32_16x16x32_bf16 v[30:33], v[134:137], v[200:203], v[30:33]
	v_mfma_f32_16x16x32_bf16 v[26:29], v[142:145], v[200:203], v[26:29]
	v_mfma_f32_16x16x32_bf16 v[14:17], v[134:137], v[216:219], v[14:17]
	v_mfma_f32_16x16x32_bf16 v[10:13], v[142:145], v[216:219], v[10:13]
	v_mfma_f32_16x16x32_bf16 v[54:57], v[146:149], v[174:177], v[54:57]
	v_mfma_f32_16x16x32_bf16 v[50:53], v[154:157], v[174:177], v[50:53]
	v_mfma_f32_16x16x32_bf16 v[38:41], v[146:149], v[188:191], v[38:41]
	v_mfma_f32_16x16x32_bf16 v[34:37], v[154:157], v[188:191], v[34:37]
	v_mfma_f32_16x16x32_bf16 v[22:25], v[146:149], v[196:199], v[22:25]
	v_mfma_f32_16x16x32_bf16 v[18:21], v[154:157], v[196:199], v[18:21]
	v_mfma_f32_16x16x32_bf16 v[6:9], v[146:149], v[204:207], v[6:9]
	v_mfma_f32_16x16x32_bf16 v[2:5], v[154:157], v[204:207], v[2:5]
	v_mfma_f32_16x16x32_bf16 v[54:57], v[150:153], v[184:187], v[54:57]
	v_mfma_f32_16x16x32_bf16 v[50:53], v[170:173], v[184:187], v[50:53]
	v_mfma_f32_16x16x32_bf16 v[38:41], v[150:153], v[192:195], v[38:41]
	v_mfma_f32_16x16x32_bf16 v[34:37], v[170:173], v[192:195], v[34:37]
	v_mfma_f32_16x16x32_bf16 v[22:25], v[150:153], v[200:203], v[22:25]
	v_mfma_f32_16x16x32_bf16 v[18:21], v[170:173], v[200:203], v[18:21]
	v_mfma_f32_16x16x32_bf16 v[6:9], v[150:153], v[216:219], v[6:9]
	v_mfma_f32_16x16x32_bf16 v[2:5], v[170:173], v[216:219], v[2:5]
	s_barrier
	s_add_i32 s49, s49, 2
	s_add_u32 s41, s41, 0x100
	s_addc_u32 s48, s48, 0
	s_add_u32 s6, s6, 0x100
	s_addc_u32 s7, s7, 0
	s_cmp_gt_u32 s49, 13
	s_cbranch_scc0 .LBB0_2626


